# P7: biases (and the up branch's +1) written into the accumulators at unit start instead of zero; the SwiGLU epilogue loses its 64 packed bias adds, bias reads and +1 adds per wave
# speedup vs baseline: 1.0135x; 1.0135x over previous
.LBB0_1195:
	s_add_u32 s26, s90, 0x7800080
	s_mov_b64 s[38:39], 0x80
	s_addc_u32 s27, s91, 0
	s_add_i32 m0, s84, 0x18000
	v_lshl_add_u64 v[8:9], v[8:9], 0, s[38:39]
	s_waitcnt vmcnt(2)
	s_barrier
	global_load_lds_dwordx4 v[8:9], off
	v_lshl_add_u64 v[6:7], v[6:7], 0, s[38:39]
	s_add_i32 m0, s84, 0x1a000
	s_add_i32 s90, s84, 0x8000
	global_load_lds_dwordx4 v[6:7], off
	v_lshl_add_u64 v[6:7], s[26:27], 0, v[156:157]
	s_mov_b32 m0, s90
	s_add_i32 s91, s84, 0xa000
	global_load_lds_dwordx4 v[6:7], off
	v_lshl_add_u64 v[6:7], s[26:27], 0, v[158:159]
	s_mov_b32 m0, s91
	v_lshl_add_u64 v[4:5], v[4:5], 0, s[38:39]
	global_load_lds_dwordx4 v[6:7], off
	s_add_i32 m0, s84, 0x1c000
	v_lshl_add_u64 v[2:3], v[2:3], 0, s[38:39]
	global_load_lds_dwordx4 v[4:5], off
	s_add_i32 m0, s84, 0x1e000
	v_and_b32_e32 v12, 48, v0
	global_load_lds_dwordx4 v[2:3], off
	v_lshlrev_b32_e32 v13, 6, v0
	s_movk_i32 s4, 0x3c0
	v_and_or_b32 v12, v13, s4, v12
	s_add_i32 s4, 0, 0x21800
	v_lshl_add_u32 v180, v10, 2, s4
	v_readlane_b32 s4, v255, 2
	s_ashr_i32 s88, s4, 3
	s_lshr_b32 s4, s15, 26
	s_lshl_b32 s0, s0, 5
	s_add_i32 s4, s14, s4
	s_and_b32 s92, s0, 0x60
	v_and_b32_e32 v11, 32, v11
	s_ashr_i32 s15, s4, 6
	s_lshl_b32 s89, s1, 6
	s_lshl_b32 s1, s1, 13
	s_lshl_b32 s0, s92, 7
	v_bitop3_b32 v10, v12, s1, v11 bitop3:0xde
	v_bitop3_b32 v157, s0, v12, v11 bitop3:0xf6
	s_cmp_gt_i32 s14, 63
	v_readlane_b32 s0, v255, 5
	s_cselect_b64 s[42:43], -1, 0
	s_cmpk_lt_u32 s7, 0x100
	v_readlane_b32 s1, v255, 6
	s_cselect_b64 s[46:47], -1, 0
	v_mov_b32_e32 v3, 0
	v_cndmask_b32_e64 v6, 0, 1, s[0:1]
	s_add_i32 s0, 0, 0x20494
	v_writelane_b32 v255, s0, 58
	s_add_i32 s0, 0, 0x2049c
	v_writelane_b32 v255, s0, 57
	s_add_i32 s0, 0, 0x204a4
	v_writelane_b32 v255, s0, 14
	s_add_i32 s0, 0, 0x204ac
	v_writelane_b32 v255, s0, 48
	s_add_i32 s0, 0, 0x204b4
	v_writelane_b32 v255, s0, 50
	s_add_i32 s0, 0, 0x204bc
	v_writelane_b32 v255, s0, 60
	s_add_i32 s0, 0, 0x204c4
	v_writelane_b32 v255, s0, 39
	s_add_i32 s0, 0, 0x204cc
	v_writelane_b32 v255, s0, 19
	s_add_i32 s0, 0, 0x204d4
	v_writelane_b32 v255, s0, 41
	s_add_i32 s0, 0, 0x204dc
	v_writelane_b32 v255, s0, 31
	s_add_i32 s0, 0, 0x204e4
	v_writelane_b32 v255, s0, 43
	s_add_i32 s0, 0, 0x204ec
	v_writelane_b32 v255, s0, 44
	s_add_i32 s0, 0, 0x204f4
	v_writelane_b32 v255, s0, 52
	s_add_i32 s0, 0, 0x204fc
	s_waitcnt vmcnt(6)
	v_mov_b32_e32 v4, v3
	v_mov_b32_e32 v5, v3
	v_writelane_b32 v255, s0, 54
	s_add_i32 s0, 0, 0x20504
	v_mov_b32_e32 v2, v3
	v_cmp_ne_u32_e64 s[4:5], 1, v6
	v_writelane_b32 v255, s0, 37
	s_add_i32 s0, 0, 0x2050c
	v_add_u32_e32 v159, 0, v10
	v_lshlrev_b32_e32 v179, 2, v1
	s_mul_i32 s25, s32, s6
	s_add_i32 s94, s15, -4
	s_add_i32 s95, s15, -2
	v_writelane_b32 v255, s0, 56
	s_add_i32 s97, 0, 0x10000
	s_add_i32 s8, 0, 0x14000
	v_mov_b32_e32 v181, 0x7a7a7a7a
	v_mov_b32_e32 v182, 0x7f7f7f7f
	s_mov_b32 s50, 0xc01d265f
	s_mov_b32 s9, 0xc0c00000
	v_mov_b32_e32 v183, 0x41000000
	v_mbcnt_lo_u32_b32 v202, -1, 0
	v_mbcnt_hi_u32_b32 v202, -1, v202
	v_ashrrev_i32_e32 v202, 4, v202
	v_lshl_add_u32 v202, v202, 3, s92
	v_lshlrev_b32_e32 v202, 2, v202
	v_add_u32_e32 v202, 0x21000, v202
	ds_read_b128 v[186:189], v202
	ds_read_b128 v[190:193], v202 offset:16
	ds_read_b128 v[194:197], v202 offset:512
	ds_read_b128 v[198:201], v202 offset:528
	s_waitcnt lgkmcnt(0)
	v_pk_add_f32 v[194:195], v[194:195], 1.0 op_sel_hi:[1,0]
	v_pk_add_f32 v[196:197], v[196:197], 1.0 op_sel_hi:[1,0]
	v_pk_add_f32 v[198:199], v[198:199], 1.0 op_sel_hi:[1,0]
	v_pk_add_f32 v[200:201], v[200:201], 1.0 op_sel_hi:[1,0]
	v_mov_b64_e32 v[6:7], v[198:199]
	v_mov_b64_e32 v[8:9], v[200:201]
	v_mov_b64_e32 v[10:11], v[194:195]
	v_mov_b64_e32 v[12:13], v[196:197]
	v_mov_b64_e32 v[14:15], v[198:199]
	v_mov_b64_e32 v[16:17], v[200:201]
	v_mov_b64_e32 v[18:19], v[194:195]
	v_mov_b64_e32 v[20:21], v[196:197]
	v_mov_b64_e32 v[22:23], v[198:199]
	v_mov_b64_e32 v[24:25], v[200:201]
	v_mov_b64_e32 v[26:27], v[194:195]
	v_mov_b64_e32 v[28:29], v[196:197]
	v_mov_b64_e32 v[30:31], v[198:199]
	v_mov_b64_e32 v[32:33], v[200:201]
	v_mov_b64_e32 v[34:35], v[194:195]
	v_mov_b64_e32 v[36:37], v[196:197]
	v_mov_b64_e32 v[38:39], v[190:191]
	v_mov_b64_e32 v[40:41], v[192:193]
	v_mov_b64_e32 v[42:43], v[186:187]
	v_mov_b64_e32 v[44:45], v[188:189]
	v_mov_b64_e32 v[46:47], v[190:191]
	v_mov_b64_e32 v[48:49], v[192:193]
	v_mov_b64_e32 v[50:51], v[186:187]
	v_mov_b64_e32 v[52:53], v[188:189]
	v_mov_b64_e32 v[54:55], v[190:191]
	v_mov_b64_e32 v[56:57], v[192:193]
	v_mov_b64_e32 v[58:59], v[186:187]
	v_mov_b64_e32 v[60:61], v[188:189]
	v_mov_b64_e32 v[62:63], v[190:191]
	v_mov_b64_e32 v[64:65], v[192:193]
	v_mov_b64_e32 v[66:67], v[186:187]
	v_mov_b64_e32 v[68:69], v[188:189]
	v_mov_b64_e32 v[70:71], v[198:199]
	v_mov_b64_e32 v[72:73], v[200:201]
	v_mov_b64_e32 v[74:75], v[194:195]
	v_mov_b64_e32 v[76:77], v[196:197]
	v_mov_b64_e32 v[78:79], v[198:199]
	v_mov_b64_e32 v[80:81], v[200:201]
	v_mov_b64_e32 v[82:83], v[194:195]
	v_mov_b64_e32 v[84:85], v[196:197]
	v_mov_b64_e32 v[86:87], v[198:199]
	v_mov_b64_e32 v[88:89], v[200:201]
	v_mov_b64_e32 v[90:91], v[194:195]
	v_mov_b64_e32 v[92:93], v[196:197]
	v_mov_b64_e32 v[94:95], v[198:199]
	v_mov_b64_e32 v[96:97], v[200:201]
	v_mov_b64_e32 v[98:99], v[194:195]
	v_mov_b64_e32 v[100:101], v[196:197]
	v_mov_b64_e32 v[102:103], v[190:191]
	v_mov_b64_e32 v[104:105], v[192:193]
	v_mov_b64_e32 v[106:107], v[186:187]
	v_mov_b64_e32 v[108:109], v[188:189]
	v_mov_b64_e32 v[110:111], v[190:191]
	v_mov_b64_e32 v[112:113], v[192:193]
	v_mov_b64_e32 v[114:115], v[186:187]
	v_mov_b64_e32 v[116:117], v[188:189]
	v_mov_b64_e32 v[118:119], v[190:191]
	v_mov_b64_e32 v[120:121], v[192:193]
	v_mov_b64_e32 v[122:123], v[186:187]
	v_mov_b64_e32 v[124:125], v[188:189]
	v_mov_b64_e32 v[126:127], v[190:191]
	v_mov_b64_e32 v[128:129], v[192:193]
	v_mov_b64_e32 v[130:131], v[186:187]
	v_mov_b64_e32 v[132:133], v[188:189]
	v_mov_b32_e32 v184, v156
	v_mov_b32_e32 v185, v158
	v_mov_b32_e32 v4, v177
	v_mov_b32_e32 v162, v178
	s_mov_b32 s96, 0
	s_barrier
	s_branch .LBB0_1198
.LBB0_1196:
	v_mov_b32_e32 v4, v3
	v_mov_b32_e32 v5, v3
	v_mov_b32_e32 v2, v3
	v_mbcnt_lo_u32_b32 v202, -1, 0
	v_mbcnt_hi_u32_b32 v202, -1, v202
	v_ashrrev_i32_e32 v202, 4, v202
	v_lshl_add_u32 v202, v202, 3, s92
	s_lshl_b32 s0, s93, 10
	s_and_b32 s0, s0, 0x400
	v_lshl_add_u32 v202, v202, 2, s0
	v_add_u32_e32 v202, 0x21000, v202
	ds_read_b128 v[186:189], v202
	ds_read_b128 v[190:193], v202 offset:16
	ds_read_b128 v[194:197], v202 offset:512
	ds_read_b128 v[198:201], v202 offset:528
	s_waitcnt lgkmcnt(0)
	v_pk_add_f32 v[194:195], v[194:195], 1.0 op_sel_hi:[1,0]
	v_pk_add_f32 v[196:197], v[196:197], 1.0 op_sel_hi:[1,0]
	v_pk_add_f32 v[198:199], v[198:199], 1.0 op_sel_hi:[1,0]
	v_pk_add_f32 v[200:201], v[200:201], 1.0 op_sel_hi:[1,0]
	v_mov_b64_e32 v[6:7], v[198:199]
	v_mov_b64_e32 v[8:9], v[200:201]
	v_mov_b64_e32 v[10:11], v[194:195]
	v_mov_b64_e32 v[12:13], v[196:197]
	v_mov_b64_e32 v[14:15], v[198:199]
	v_mov_b64_e32 v[16:17], v[200:201]
	v_mov_b64_e32 v[18:19], v[194:195]
	v_mov_b64_e32 v[20:21], v[196:197]
	v_mov_b64_e32 v[22:23], v[198:199]
	v_mov_b64_e32 v[24:25], v[200:201]
	v_mov_b64_e32 v[26:27], v[194:195]
	v_mov_b64_e32 v[28:29], v[196:197]
	v_mov_b64_e32 v[30:31], v[198:199]
	v_mov_b64_e32 v[32:33], v[200:201]
	v_mov_b64_e32 v[34:35], v[194:195]
	v_mov_b64_e32 v[36:37], v[196:197]
	v_mov_b64_e32 v[38:39], v[190:191]
	v_mov_b64_e32 v[40:41], v[192:193]
	v_mov_b64_e32 v[42:43], v[186:187]
	v_mov_b64_e32 v[44:45], v[188:189]
	v_mov_b64_e32 v[46:47], v[190:191]
	v_mov_b64_e32 v[48:49], v[192:193]
	v_mov_b64_e32 v[50:51], v[186:187]
	v_mov_b64_e32 v[52:53], v[188:189]
	v_mov_b64_e32 v[54:55], v[190:191]
	v_mov_b64_e32 v[56:57], v[192:193]
	v_mov_b64_e32 v[58:59], v[186:187]
	v_mov_b64_e32 v[60:61], v[188:189]
	v_mov_b64_e32 v[62:63], v[190:191]
	v_mov_b64_e32 v[64:65], v[192:193]
	v_mov_b64_e32 v[66:67], v[186:187]
	v_mov_b64_e32 v[68:69], v[188:189]
	v_mov_b64_e32 v[70:71], v[198:199]
	v_mov_b64_e32 v[72:73], v[200:201]
	v_mov_b64_e32 v[74:75], v[194:195]
	v_mov_b64_e32 v[76:77], v[196:197]
	v_mov_b64_e32 v[78:79], v[198:199]
	v_mov_b64_e32 v[80:81], v[200:201]
	v_mov_b64_e32 v[82:83], v[194:195]
	v_mov_b64_e32 v[84:85], v[196:197]
	v_mov_b64_e32 v[86:87], v[198:199]
	v_mov_b64_e32 v[88:89], v[200:201]
	v_mov_b64_e32 v[90:91], v[194:195]
	v_mov_b64_e32 v[92:93], v[196:197]
	v_mov_b64_e32 v[94:95], v[198:199]
	v_mov_b64_e32 v[96:97], v[200:201]
	v_mov_b64_e32 v[98:99], v[194:195]
	v_mov_b64_e32 v[100:101], v[196:197]
	v_mov_b64_e32 v[102:103], v[190:191]
	v_mov_b64_e32 v[104:105], v[192:193]
	v_mov_b64_e32 v[106:107], v[186:187]
	v_mov_b64_e32 v[108:109], v[188:189]
	v_mov_b64_e32 v[110:111], v[190:191]
	v_mov_b64_e32 v[112:113], v[192:193]
	v_mov_b64_e32 v[114:115], v[186:187]
	v_mov_b64_e32 v[116:117], v[188:189]
	v_mov_b64_e32 v[118:119], v[190:191]
	v_mov_b64_e32 v[120:121], v[192:193]
	v_mov_b64_e32 v[122:123], v[186:187]
	v_mov_b64_e32 v[124:125], v[188:189]
	v_mov_b64_e32 v[126:127], v[190:191]
	v_mov_b64_e32 v[128:129], v[192:193]
	v_mov_b64_e32 v[130:131], v[186:187]
	v_mov_b64_e32 v[132:133], v[188:189]
	v_mov_b32_e32 v184, v156
	v_mov_b32_e32 v185, v158
	v_mov_b32_e32 v4, v177
	v_mov_b32_e32 v162, v178
	s_mov_b32 s68, s12
	s_mov_b32 s33, s82
	s_mov_b32 s69, s13
	s_mov_b64 s[20:21], s[76:77]
	s_mov_b32 s96, s93

.Lp7pub_skip:
	s_nop 15
	s_nop 15
	s_lshl_b32 s0, s96, 10
	s_and_b32 s0, s0, 0x400
	v_mbcnt_lo_u32_b32 v2, -1, 0
	v_mbcnt_hi_u32_b32 v2, -1, v2
	s_add_i32 s0, s0, 0
	v_ashrrev_i32_e32 v5, 4, v2
	v_lshl_add_u32 v134, v5, 3, s92
	v_lshl_add_u32 v135, v134, 2, s0
	s_lshr_b32 s0, s33, 1
	s_and_b32 s0, s0, 0x380
	v_add_u32_e32 v151, 0x21000, v135
	v_add_u32_e32 v164, s0, v134
	v_and_b32_e32 v5, 1, v5
	v_and_or_b32 v2, v2, 15, s89
	v_ashrrev_i32_e32 v165, 31, v164
	s_waitcnt lgkmcnt(0)
	v_med3_f32 v192, v98, s9, v183
	s_waitcnt lgkmcnt(0)
	v_lshlrev_b32_e32 v142, 3, v5
	v_ashrrev_i32_e32 v143, 31, v142
	v_sub_co_u32_e32 v166, vcc, 0, v142
	s_nop 0
	v_subb_co_u32_e32 v167, vcc, 0, v143, vcc
	v_med3_f32 v193, v99, s9, v183
	v_min_f32_e32 v144, 0x40e00000, v130
	v_min_f32_e32 v145, 0x40e00000, v131
	v_min_f32_e32 v142, 0x40e00000, v132
	v_min_f32_e32 v143, 0x40e00000, v133
	v_pk_mul_f32 v[198:199], v[144:145], s[50:51] op_sel_hi:[1,0]
	v_pk_mul_f32 v[144:145], v[144:145], v[192:193]
	v_pk_mul_f32 v[192:193], v[142:143], s[50:51] op_sel_hi:[1,0]
	v_med3_f32 v190, v100, s9, v183
	v_exp_f32_e32 v192, v192
	v_exp_f32_e32 v193, v193
	v_med3_f32 v191, v101, s9, v183
	v_pk_mul_f32 v[142:143], v[142:143], v[190:191]
	v_pk_add_f32 v[192:193], v[192:193], 1.0 op_sel_hi:[1,0]
	v_rcp_f32_e32 v192, v192
	v_rcp_f32_e32 v193, v193
	v_exp_f32_e32 v198, v198
	v_exp_f32_e32 v199, v199
	v_pk_mul_f32 v[190:191], v[142:143], v[192:193]
	v_min_f32_e32 v142, 0x40e00000, v126
	v_min_f32_e32 v143, 0x40e00000, v127
	v_pk_mul_f32 v[188:189], v[142:143], s[50:51] op_sel_hi:[1,0]
	v_med3_f32 v192, v94, s9, v183
	v_exp_f32_e32 v188, v188
	v_exp_f32_e32 v189, v189
	v_med3_f32 v193, v95, s9, v183
	v_pk_mul_f32 v[142:143], v[142:143], v[192:193]
	v_med3_f32 v192, v96, s9, v183
	v_pk_add_f32 v[188:189], v[188:189], 1.0 op_sel_hi:[1,0]
	v_med3_f32 v193, v97, s9, v183
	v_rcp_f32_e32 v188, v188
	v_rcp_f32_e32 v189, v189
	v_pk_add_f32 v[198:199], v[198:199], 1.0 op_sel_hi:[1,0]
	v_rcp_f32_e32 v198, v198
	v_pk_mul_f32 v[188:189], v[142:143], v[188:189]
	v_min_f32_e32 v142, 0x40e00000, v128
	v_min_f32_e32 v143, 0x40e00000, v129
	v_pk_mul_f32 v[186:187], v[142:143], s[50:51] op_sel_hi:[1,0]
	v_pk_mul_f32 v[142:143], v[142:143], v[192:193]
	v_exp_f32_e32 v186, v186
	v_exp_f32_e32 v187, v187
	v_rcp_f32_e32 v199, v199
	v_med3_f32 v194, v90, s9, v183
	v_med3_f32 v195, v91, s9, v183
	v_pk_add_f32 v[186:187], v[186:187], 1.0 op_sel_hi:[1,0]
	v_pk_mul_f32 v[144:145], v[144:145], v[198:199]
	v_rcp_f32_e32 v186, v186
	v_rcp_f32_e32 v187, v187
	v_med3_f32 v192, v92, s9, v183
	v_pk_mul_f32 v[186:187], v[142:143], v[186:187]
	v_mov_b32_e32 v143, v3
	v_cvt_pk_fp8_f32 v143, v188, v189
	v_mov_b32_e32 v142, v3
	v_cvt_pk_fp8_f32 v142, v144, v145
	v_cvt_pk_fp8_f32 v143, v186, v187 op_sel:[0,0,1]
	v_min_f32_e32 v144, 0x40e00000, v124
	v_min_f32_e32 v186, 0x40e00000, v122
	v_min_f32_e32 v187, 0x40e00000, v123
	v_min_f32_e32 v145, 0x40e00000, v125
	v_pk_mul_f32 v[200:201], v[186:187], s[50:51] op_sel_hi:[1,0]
	v_pk_mul_f32 v[186:187], v[186:187], v[194:195]
	v_pk_mul_f32 v[194:195], v[144:145], s[50:51] op_sel_hi:[1,0]
	v_med3_f32 v193, v93, s9, v183
	v_exp_f32_e32 v194, v194
	v_exp_f32_e32 v195, v195
	v_cvt_pk_fp8_f32 v142, v190, v191 op_sel:[0,0,1]
	v_pk_mul_f32 v[144:145], v[144:145], v[192:193]
	v_pk_add_f32 v[194:195], v[194:195], 1.0 op_sel_hi:[1,0]
	v_rcp_f32_e32 v194, v194
	v_rcp_f32_e32 v195, v195
	v_exp_f32_e32 v200, v200
	v_exp_f32_e32 v201, v201
	v_pk_mul_f32 v[192:193], v[144:145], v[194:195]
	v_min_f32_e32 v144, 0x40e00000, v118
	v_min_f32_e32 v145, 0x40e00000, v119
	v_pk_mul_f32 v[190:191], v[144:145], s[50:51] op_sel_hi:[1,0]
	v_med3_f32 v194, v86, s9, v183
	v_exp_f32_e32 v190, v190
	v_exp_f32_e32 v191, v191
	v_med3_f32 v195, v87, s9, v183
	v_pk_mul_f32 v[144:145], v[144:145], v[194:195]
	v_pk_add_f32 v[200:201], v[200:201], 1.0 op_sel_hi:[1,0]
	v_pk_add_f32 v[190:191], v[190:191], 1.0 op_sel_hi:[1,0]
	v_rcp_f32_e32 v200, v200
	v_rcp_f32_e32 v190, v190
	v_rcp_f32_e32 v191, v191
	v_rcp_f32_e32 v201, v201
	v_med3_f32 v194, v88, s9, v183
	v_med3_f32 v195, v89, s9, v183
	v_pk_mul_f32 v[190:191], v[144:145], v[190:191]
	v_min_f32_e32 v144, 0x40e00000, v120
	v_min_f32_e32 v145, 0x40e00000, v121
	v_pk_mul_f32 v[188:189], v[144:145], s[50:51] op_sel_hi:[1,0]
	v_pk_mul_f32 v[144:145], v[144:145], v[194:195]
	v_exp_f32_e32 v188, v188
	v_exp_f32_e32 v189, v189
	v_pk_mul_f32 v[186:187], v[186:187], v[200:201]
	v_lshlrev_b32_e32 v5, 4, v5
	v_add_u32_e32 v151, v5, v2
	v_pk_add_f32 v[188:189], v[188:189], 1.0 op_sel_hi:[1,0]
	v_cmp_gt_i32_e32 vcc, s68, v151
	v_rcp_f32_e32 v188, v188
	v_rcp_f32_e32 v189, v189
	s_nop 0
	v_pk_mul_f32 v[188:189], v[144:145], v[188:189]
	v_mov_b32_e32 v144, v3
	v_mov_b32_e32 v145, v3
	v_cvt_pk_fp8_f32 v144, v186, v187
	v_cvt_pk_fp8_f32 v145, v190, v191
	v_cvt_pk_fp8_f32 v144, v192, v193 op_sel:[0,0,1]
	v_cvt_pk_fp8_f32 v145, v188, v189 op_sel:[0,0,1]
	s_nop 0
	v_permlane16_swap_b32_e32 v142, v144
	v_permlane16_swap_b32_e32 v143, v145
	s_and_saveexec_b64 s[0:1], vcc
	s_cbranch_execz .LBB0_1222
	v_add_u32_e32 v186, s69, v151
	v_ashrrev_i32_e32 v187, 31, v186
	v_lshlrev_b64 v[186:187], 10, v[186:187]
	v_lshl_add_u64 v[186:187], s[10:11], 0, v[186:187]
	v_lshl_add_u64 v[186:187], v[186:187], 0, v[164:165]
	v_lshl_add_u64 v[186:187], v[186:187], 0, v[166:167]
	global_store_dwordx4 v[186:187], v[142:145], off
.LBB0_1222:
	s_or_b64 exec, exec, s[0:1]
	s_nop 0
	v_min_f32_e32 v144, 0x40e00000, v114
	v_min_f32_e32 v145, 0x40e00000, v115
	v_med3_f32 v192, v82, s9, v183
	v_med3_f32 v193, v83, s9, v183
	v_min_f32_e32 v142, 0x40e00000, v116
	v_min_f32_e32 v143, 0x40e00000, v117
	v_pk_mul_f32 v[198:199], v[144:145], s[50:51] op_sel_hi:[1,0]
	v_pk_mul_f32 v[144:145], v[144:145], v[192:193]
	v_pk_mul_f32 v[192:193], v[142:143], s[50:51] op_sel_hi:[1,0]
	v_exp_f32_e32 v192, v192
	v_exp_f32_e32 v193, v193
	v_med3_f32 v190, v84, s9, v183
	v_med3_f32 v191, v85, s9, v183
	v_pk_add_f32 v[192:193], v[192:193], 1.0 op_sel_hi:[1,0]
	v_pk_mul_f32 v[142:143], v[142:143], v[190:191]
	v_rcp_f32_e32 v192, v192
	v_rcp_f32_e32 v193, v193
	v_exp_f32_e32 v198, v198
	v_pk_mul_f32 v[190:191], v[142:143], v[192:193]
	v_min_f32_e32 v142, 0x40e00000, v110
	v_min_f32_e32 v143, 0x40e00000, v111
	v_pk_mul_f32 v[188:189], v[142:143], s[50:51] op_sel_hi:[1,0]
	v_med3_f32 v192, v78, s9, v183
	v_exp_f32_e32 v188, v188
	v_exp_f32_e32 v189, v189
	v_med3_f32 v193, v79, s9, v183
	v_pk_mul_f32 v[142:143], v[142:143], v[192:193]
	v_exp_f32_e32 v199, v199
	v_pk_add_f32 v[188:189], v[188:189], 1.0 op_sel_hi:[1,0]
	v_rcp_f32_e32 v188, v188
	v_rcp_f32_e32 v189, v189
	v_med3_f32 v192, v80, s9, v183
	v_med3_f32 v193, v81, s9, v183
	v_pk_add_f32 v[198:199], v[198:199], 1.0 op_sel_hi:[1,0]
	v_pk_mul_f32 v[188:189], v[142:143], v[188:189]
	v_min_f32_e32 v142, 0x40e00000, v112
	v_min_f32_e32 v143, 0x40e00000, v113
	v_pk_mul_f32 v[186:187], v[142:143], s[50:51] op_sel_hi:[1,0]
	v_pk_mul_f32 v[142:143], v[142:143], v[192:193]
	v_exp_f32_e32 v186, v186
	v_exp_f32_e32 v187, v187
	v_rcp_f32_e32 v198, v198
	v_rcp_f32_e32 v199, v199
	v_pk_add_f32 v[186:187], v[186:187], 1.0 op_sel_hi:[1,0]
	v_med3_f32 v194, v74, s9, v183
	v_rcp_f32_e32 v186, v186
	v_rcp_f32_e32 v187, v187
	v_pk_mul_f32 v[144:145], v[144:145], v[198:199]
	v_med3_f32 v195, v75, s9, v183
	v_pk_mul_f32 v[186:187], v[142:143], v[186:187]
	v_mov_b32_e32 v143, v3
	v_cvt_pk_fp8_f32 v143, v188, v189
	v_mov_b32_e32 v142, v3
	v_cvt_pk_fp8_f32 v142, v144, v145
	v_cvt_pk_fp8_f32 v143, v186, v187 op_sel:[0,0,1]
	v_min_f32_e32 v144, 0x40e00000, v108
	v_min_f32_e32 v186, 0x40e00000, v106
	v_min_f32_e32 v187, 0x40e00000, v107
	v_min_f32_e32 v145, 0x40e00000, v109
	v_pk_mul_f32 v[200:201], v[186:187], s[50:51] op_sel_hi:[1,0]
	v_pk_mul_f32 v[186:187], v[186:187], v[194:195]
	v_pk_mul_f32 v[194:195], v[144:145], s[50:51] op_sel_hi:[1,0]
	v_med3_f32 v192, v76, s9, v183
	v_exp_f32_e32 v194, v194
	v_exp_f32_e32 v195, v195
	v_med3_f32 v193, v77, s9, v183
	v_cvt_pk_fp8_f32 v142, v190, v191 op_sel:[0,0,1]
	v_pk_add_f32 v[194:195], v[194:195], 1.0 op_sel_hi:[1,0]
	v_pk_mul_f32 v[144:145], v[144:145], v[192:193]
	v_rcp_f32_e32 v194, v194
	v_rcp_f32_e32 v195, v195
	v_exp_f32_e32 v200, v200
	v_pk_mul_f32 v[192:193], v[144:145], v[194:195]
	v_min_f32_e32 v144, 0x40e00000, v102
	v_min_f32_e32 v145, 0x40e00000, v103
	v_pk_mul_f32 v[190:191], v[144:145], s[50:51] op_sel_hi:[1,0]
	v_med3_f32 v194, v70, s9, v183
	v_exp_f32_e32 v190, v190
	v_exp_f32_e32 v191, v191
	v_med3_f32 v195, v71, s9, v183
	v_pk_mul_f32 v[144:145], v[144:145], v[194:195]
	v_exp_f32_e32 v201, v201
	v_pk_add_f32 v[190:191], v[190:191], 1.0 op_sel_hi:[1,0]
	v_rcp_f32_e32 v190, v190
	v_rcp_f32_e32 v191, v191
	v_pk_add_f32 v[200:201], v[200:201], 1.0 op_sel_hi:[1,0]
	v_med3_f32 v194, v72, s9, v183
	v_rcp_f32_e32 v200, v200
	v_pk_mul_f32 v[190:191], v[144:145], v[190:191]
	v_min_f32_e32 v144, 0x40e00000, v104
	v_min_f32_e32 v145, 0x40e00000, v105
	v_pk_mul_f32 v[188:189], v[144:145], s[50:51] op_sel_hi:[1,0]
	v_rcp_f32_e32 v201, v201
	v_exp_f32_e32 v188, v188
	v_exp_f32_e32 v189, v189
	v_med3_f32 v195, v73, s9, v183
	v_pk_mul_f32 v[144:145], v[144:145], v[194:195]
	v_pk_mul_f32 v[186:187], v[186:187], v[200:201]
	v_pk_add_f32 v[188:189], v[188:189], 1.0 op_sel_hi:[1,0]
	v_add_u32_e32 v151, 32, v5
	v_rcp_f32_e32 v188, v188
	v_rcp_f32_e32 v189, v189
	v_add_u32_e32 v163, v151, v2
	v_cmp_gt_i32_e32 vcc, s68, v163
	v_pk_mul_f32 v[188:189], v[144:145], v[188:189]
	v_mov_b32_e32 v144, v3
	v_mov_b32_e32 v145, v3
	v_cvt_pk_fp8_f32 v144, v186, v187
	v_cvt_pk_fp8_f32 v145, v190, v191
	v_cvt_pk_fp8_f32 v144, v192, v193 op_sel:[0,0,1]
	v_cvt_pk_fp8_f32 v145, v188, v189 op_sel:[0,0,1]
	s_nop 0
	v_permlane16_swap_b32_e32 v142, v144
	v_permlane16_swap_b32_e32 v143, v145
	s_and_saveexec_b64 s[0:1], vcc
	s_cbranch_execz .LBB0_1224
	v_add_u32_e32 v186, s69, v163
	v_ashrrev_i32_e32 v187, 31, v186
	v_lshlrev_b64 v[186:187], 10, v[186:187]
	v_lshl_add_u64 v[186:187], s[10:11], 0, v[186:187]
	v_lshl_add_u64 v[186:187], v[186:187], 0, v[164:165]
	v_lshl_add_u64 v[186:187], v[186:187], 0, v[166:167]
	global_store_dwordx4 v[186:187], v[142:145], off
.LBB0_1224:
	s_or_b64 exec, exec, s[0:1]
	s_nop 0
	v_min_f32_e32 v144, 0x40e00000, v66
	v_min_f32_e32 v145, 0x40e00000, v67
	v_med3_f32 v192, v34, s9, v183
	v_med3_f32 v193, v35, s9, v183
	v_min_f32_e32 v142, 0x40e00000, v68
	v_min_f32_e32 v143, 0x40e00000, v69
	v_pk_mul_f32 v[198:199], v[144:145], s[50:51] op_sel_hi:[1,0]
	v_pk_mul_f32 v[144:145], v[144:145], v[192:193]
	v_pk_mul_f32 v[192:193], v[142:143], s[50:51] op_sel_hi:[1,0]
	v_exp_f32_e32 v192, v192
	v_exp_f32_e32 v193, v193
	v_med3_f32 v190, v36, s9, v183
	v_med3_f32 v191, v37, s9, v183
	v_pk_add_f32 v[192:193], v[192:193], 1.0 op_sel_hi:[1,0]
	v_pk_mul_f32 v[142:143], v[142:143], v[190:191]
	v_rcp_f32_e32 v192, v192
	v_rcp_f32_e32 v193, v193
	v_exp_f32_e32 v198, v198
	v_pk_mul_f32 v[190:191], v[142:143], v[192:193]
	v_min_f32_e32 v142, 0x40e00000, v62
	v_min_f32_e32 v143, 0x40e00000, v63
	v_pk_mul_f32 v[188:189], v[142:143], s[50:51] op_sel_hi:[1,0]
	v_med3_f32 v192, v30, s9, v183
	v_exp_f32_e32 v188, v188
	v_exp_f32_e32 v189, v189
	v_med3_f32 v193, v31, s9, v183
	v_pk_mul_f32 v[142:143], v[142:143], v[192:193]
	v_exp_f32_e32 v199, v199
	v_pk_add_f32 v[188:189], v[188:189], 1.0 op_sel_hi:[1,0]
	v_rcp_f32_e32 v188, v188
	v_rcp_f32_e32 v189, v189
	v_med3_f32 v192, v32, s9, v183
	v_med3_f32 v193, v33, s9, v183
	v_pk_add_f32 v[198:199], v[198:199], 1.0 op_sel_hi:[1,0]
	v_pk_mul_f32 v[188:189], v[142:143], v[188:189]
	v_min_f32_e32 v142, 0x40e00000, v64
	v_min_f32_e32 v143, 0x40e00000, v65
	v_pk_mul_f32 v[186:187], v[142:143], s[50:51] op_sel_hi:[1,0]
	v_pk_mul_f32 v[142:143], v[142:143], v[192:193]
	v_exp_f32_e32 v186, v186
	v_exp_f32_e32 v187, v187
	v_rcp_f32_e32 v198, v198
	v_rcp_f32_e32 v199, v199
	v_pk_add_f32 v[186:187], v[186:187], 1.0 op_sel_hi:[1,0]
	v_med3_f32 v194, v26, s9, v183
	v_rcp_f32_e32 v186, v186
	v_rcp_f32_e32 v187, v187
	v_pk_mul_f32 v[144:145], v[144:145], v[198:199]
	v_med3_f32 v195, v27, s9, v183
	v_pk_mul_f32 v[186:187], v[142:143], v[186:187]
	v_mov_b32_e32 v143, v3
	v_cvt_pk_fp8_f32 v143, v188, v189
	v_mov_b32_e32 v142, v3
	v_cvt_pk_fp8_f32 v142, v144, v145
	v_cvt_pk_fp8_f32 v143, v186, v187 op_sel:[0,0,1]
	v_min_f32_e32 v144, 0x40e00000, v60
	v_min_f32_e32 v186, 0x40e00000, v58
	v_min_f32_e32 v187, 0x40e00000, v59
	v_min_f32_e32 v145, 0x40e00000, v61
	v_pk_mul_f32 v[200:201], v[186:187], s[50:51] op_sel_hi:[1,0]
	v_pk_mul_f32 v[186:187], v[186:187], v[194:195]
	v_pk_mul_f32 v[194:195], v[144:145], s[50:51] op_sel_hi:[1,0]
	v_med3_f32 v192, v28, s9, v183
	v_exp_f32_e32 v194, v194
	v_exp_f32_e32 v195, v195
	v_med3_f32 v193, v29, s9, v183
	v_cvt_pk_fp8_f32 v142, v190, v191 op_sel:[0,0,1]
	v_pk_add_f32 v[194:195], v[194:195], 1.0 op_sel_hi:[1,0]
	v_pk_mul_f32 v[144:145], v[144:145], v[192:193]
	v_rcp_f32_e32 v194, v194
	v_rcp_f32_e32 v195, v195
	v_exp_f32_e32 v200, v200
	v_pk_mul_f32 v[192:193], v[144:145], v[194:195]
	v_min_f32_e32 v144, 0x40e00000, v54
	v_min_f32_e32 v145, 0x40e00000, v55
	v_pk_mul_f32 v[190:191], v[144:145], s[50:51] op_sel_hi:[1,0]
	v_med3_f32 v194, v22, s9, v183
	v_exp_f32_e32 v190, v190
	v_exp_f32_e32 v191, v191
	v_med3_f32 v195, v23, s9, v183
	v_pk_mul_f32 v[144:145], v[144:145], v[194:195]
	v_exp_f32_e32 v201, v201
	v_pk_add_f32 v[190:191], v[190:191], 1.0 op_sel_hi:[1,0]
	v_rcp_f32_e32 v190, v190
	v_rcp_f32_e32 v191, v191
	v_pk_add_f32 v[200:201], v[200:201], 1.0 op_sel_hi:[1,0]
	v_med3_f32 v194, v24, s9, v183
	v_rcp_f32_e32 v200, v200
	v_pk_mul_f32 v[190:191], v[144:145], v[190:191]
	v_min_f32_e32 v144, 0x40e00000, v56
	v_min_f32_e32 v145, 0x40e00000, v57
	v_pk_mul_f32 v[188:189], v[144:145], s[50:51] op_sel_hi:[1,0]
	v_rcp_f32_e32 v201, v201
	v_exp_f32_e32 v188, v188
	v_exp_f32_e32 v189, v189
	v_med3_f32 v195, v25, s9, v183
	v_pk_mul_f32 v[144:145], v[144:145], v[194:195]
	v_pk_mul_f32 v[186:187], v[186:187], v[200:201]
	v_pk_add_f32 v[188:189], v[188:189], 1.0 op_sel_hi:[1,0]
	v_add_u32_e32 v2, 0x80, v2
	v_rcp_f32_e32 v188, v188
	v_rcp_f32_e32 v189, v189
	v_add_u32_e32 v5, v5, v2
	v_cmp_gt_i32_e32 vcc, s68, v5
	v_pk_mul_f32 v[188:189], v[144:145], v[188:189]
	v_mov_b32_e32 v144, v3
	v_mov_b32_e32 v145, v3
	v_cvt_pk_fp8_f32 v144, v186, v187
	v_cvt_pk_fp8_f32 v145, v190, v191
	v_cvt_pk_fp8_f32 v144, v192, v193 op_sel:[0,0,1]
	v_cvt_pk_fp8_f32 v145, v188, v189 op_sel:[0,0,1]
	s_nop 0
	v_permlane16_swap_b32_e32 v142, v144
	v_permlane16_swap_b32_e32 v143, v145
	s_and_saveexec_b64 s[0:1], vcc
	s_cbranch_execz .LBB0_1226
	v_add_u32_e32 v186, s69, v5
	v_ashrrev_i32_e32 v187, 31, v186
	v_lshlrev_b64 v[186:187], 10, v[186:187]
	v_lshl_add_u64 v[186:187], s[10:11], 0, v[186:187]
	v_lshl_add_u64 v[186:187], v[186:187], 0, v[164:165]
	v_lshl_add_u64 v[186:187], v[186:187], 0, v[166:167]
	global_store_dwordx4 v[186:187], v[142:145], off
.LBB0_1226:
	s_or_b64 exec, exec, s[0:1]
	s_nop 0
	v_min_f32_e32 v144, 0x40e00000, v50
	v_min_f32_e32 v145, 0x40e00000, v51
	v_med3_f32 v192, v18, s9, v183
	v_med3_f32 v193, v19, s9, v183
	v_min_f32_e32 v142, 0x40e00000, v52
	v_min_f32_e32 v143, 0x40e00000, v53
	v_pk_mul_f32 v[198:199], v[144:145], s[50:51] op_sel_hi:[1,0]
	v_pk_mul_f32 v[144:145], v[144:145], v[192:193]
	v_pk_mul_f32 v[192:193], v[142:143], s[50:51] op_sel_hi:[1,0]
	v_exp_f32_e32 v192, v192
	v_exp_f32_e32 v193, v193
	v_med3_f32 v190, v20, s9, v183
	v_med3_f32 v191, v21, s9, v183
	v_pk_add_f32 v[192:193], v[192:193], 1.0 op_sel_hi:[1,0]
	v_pk_mul_f32 v[142:143], v[142:143], v[190:191]
	v_rcp_f32_e32 v192, v192
	v_rcp_f32_e32 v193, v193
	v_exp_f32_e32 v198, v198
	v_pk_mul_f32 v[190:191], v[142:143], v[192:193]
	v_min_f32_e32 v142, 0x40e00000, v46
	v_min_f32_e32 v143, 0x40e00000, v47
	v_pk_mul_f32 v[188:189], v[142:143], s[50:51] op_sel_hi:[1,0]
	v_med3_f32 v192, v14, s9, v183
	v_exp_f32_e32 v188, v188
	v_exp_f32_e32 v189, v189
	v_med3_f32 v193, v15, s9, v183
	v_pk_mul_f32 v[142:143], v[142:143], v[192:193]
	v_exp_f32_e32 v199, v199
	v_pk_add_f32 v[188:189], v[188:189], 1.0 op_sel_hi:[1,0]
	v_rcp_f32_e32 v188, v188
	v_rcp_f32_e32 v189, v189
	v_pk_add_f32 v[198:199], v[198:199], 1.0 op_sel_hi:[1,0]
	v_med3_f32 v192, v16, s9, v183
	v_rcp_f32_e32 v198, v198
	v_pk_mul_f32 v[188:189], v[142:143], v[188:189]
	v_min_f32_e32 v142, 0x40e00000, v48
	v_min_f32_e32 v143, 0x40e00000, v49
	v_pk_mul_f32 v[186:187], v[142:143], s[50:51] op_sel_hi:[1,0]
	v_rcp_f32_e32 v199, v199
	v_exp_f32_e32 v186, v186
	v_exp_f32_e32 v187, v187
	v_med3_f32 v193, v17, s9, v183
	v_pk_mul_f32 v[142:143], v[142:143], v[192:193]
	v_pk_mul_f32 v[144:145], v[144:145], v[198:199]
	v_pk_add_f32 v[186:187], v[186:187], 1.0 op_sel_hi:[1,0]
	v_rcp_f32_e32 v186, v186
	v_rcp_f32_e32 v187, v187
	v_min_f32_e32 v140, 0x40e00000, v44
	v_min_f32_e32 v138, 0x40e00000, v42
	v_pk_mul_f32 v[186:187], v[142:143], v[186:187]
	v_mov_b32_e32 v142, v3
	v_cvt_pk_fp8_f32 v142, v144, v145
	v_min_f32_e32 v139, 0x40e00000, v43
	v_med3_f32 v168, v10, s9, v183
	v_med3_f32 v169, v11, s9, v183
	v_min_f32_e32 v141, 0x40e00000, v45
	v_pk_mul_f32 v[174:175], v[138:139], s[50:51] op_sel_hi:[1,0]
	v_pk_mul_f32 v[138:139], v[138:139], v[168:169]
	v_pk_mul_f32 v[168:169], v[140:141], s[50:51] op_sel_hi:[1,0]
	v_med3_f32 v144, v12, s9, v183
	v_exp_f32_e32 v168, v168
	v_exp_f32_e32 v169, v169
	v_med3_f32 v145, v13, s9, v183
	v_min_f32_e32 v134, 0x40e00000, v38
	v_min_f32_e32 v135, 0x40e00000, v39
	v_pk_mul_f32 v[140:141], v[140:141], v[144:145]
	v_pk_mul_f32 v[144:145], v[134:135], s[50:51] op_sel_hi:[1,0]
	v_pk_add_f32 v[168:169], v[168:169], 1.0 op_sel_hi:[1,0]
	v_exp_f32_e32 v144, v144
	v_exp_f32_e32 v145, v145
	v_rcp_f32_e32 v168, v168
	v_rcp_f32_e32 v169, v169
	v_pk_add_f32 v[144:145], v[144:145], 1.0 op_sel_hi:[1,0]
	v_min_f32_e32 v136, 0x40e00000, v40
	v_rcp_f32_e32 v144, v144
	v_rcp_f32_e32 v145, v145
	v_pk_mul_f32 v[140:141], v[140:141], v[168:169]
	v_med3_f32 v168, v6, s9, v183
	v_med3_f32 v169, v7, s9, v183
	v_pk_mul_f32 v[134:135], v[134:135], v[168:169]
	v_min_f32_e32 v137, 0x40e00000, v41
	v_pk_mul_f32 v[134:135], v[134:135], v[144:145]
	v_pk_mul_f32 v[144:145], v[136:137], s[50:51] op_sel_hi:[1,0]
	v_exp_f32_e32 v174, v174
	v_exp_f32_e32 v175, v175
	v_exp_f32_e32 v144, v144
	v_exp_f32_e32 v145, v145
	v_med3_f32 v168, v8, s9, v183
	v_pk_add_f32 v[174:175], v[174:175], 1.0 op_sel_hi:[1,0]
	v_med3_f32 v169, v9, s9, v183
	v_pk_add_f32 v[144:145], v[144:145], 1.0 op_sel_hi:[1,0]
	v_rcp_f32_e32 v174, v174
	v_rcp_f32_e32 v175, v175
	v_rcp_f32_e32 v144, v144
	v_rcp_f32_e32 v145, v145
	v_pk_mul_f32 v[136:137], v[136:137], v[168:169]
	v_mov_b32_e32 v143, v3
	v_pk_mul_f32 v[138:139], v[138:139], v[174:175]
	v_pk_mul_f32 v[136:137], v[136:137], v[144:145]
	v_mov_b32_e32 v144, v3
	v_mov_b32_e32 v145, v3
	v_cvt_pk_fp8_f32 v143, v188, v189
	v_cvt_pk_fp8_f32 v144, v138, v139
	v_cvt_pk_fp8_f32 v145, v134, v135
	v_cvt_pk_fp8_f32 v142, v190, v191 op_sel:[0,0,1]
	v_cvt_pk_fp8_f32 v143, v186, v187 op_sel:[0,0,1]
	v_cvt_pk_fp8_f32 v144, v140, v141 op_sel:[0,0,1]
	v_cvt_pk_fp8_f32 v145, v136, v137 op_sel:[0,0,1]
	v_add_u32_e32 v2, v151, v2
	v_cmp_gt_i32_e32 vcc, s68, v2
	v_permlane16_swap_b32_e32 v142, v144
	v_permlane16_swap_b32_e32 v143, v145
	s_and_saveexec_b64 s[0:1], vcc
	s_cbranch_execnz .LBB0_1228
	s_or_b64 exec, exec, s[0:1]
	s_andn2_b64 vcc, exec, s[74:75]
	s_cbranch_vccnz .LBB0_1197
	s_branch .LBB0_1229
